# baseline (speedup 1.0000x reference)
_Z11proj_kernelPKfS0_S0_PKDF16_S0_S0_S0_PDF16_S3_S3_Pj:
	s_ashr_i32 s12, s2, 6
	s_load_dwordx8 s[4:11], s[0:1], 0x0
	s_cmp_gt_u32 s2, 63
	s_cselect_b64 s[22:23], -1, 0
	s_cmp_lg_u32 s12, 1
	s_cselect_b64 s[18:19], -1, 0
	s_cmp_eq_u32 s12, 1
	s_cselect_b64 s[20:21], -1, 0
	s_and_b64 s[14:15], s[20:21], exec
	s_waitcnt lgkmcnt(0)
	s_cselect_b32 s14, s6, s8
	s_cselect_b32 s15, s7, s9
	s_ashr_i32 s13, s12, 31
	s_lshl_b32 s28, s2, 7
	s_lshl_b64 s[6:7], s[12:13], 19
	s_and_b32 s3, s28, 0x1f80
	s_cmp_lt_u32 s2, 64
	s_cselect_b64 vcc, -1, 0
	v_lshrrev_b32_e32 v1, 2, v0
	v_lshrrev_b32_e32 v2, 2, v0
	v_and_b32_e32 v2, 0x70, v2
	v_bfe_u32 v254, v0, 3, 3
	v_or_b32_e32 v254, v2, v254
	v_or_b32_e32 v2, s3, v254
	s_and_b64 s[8:9], vcc, exec
	s_cselect_b32 s25, s5, s15
	s_cselect_b32 s24, s4, s14
	v_lshlrev_b32_e32 v2, 11, v2
	v_mov_b32_e32 v3, 0
	v_lshlrev_b32_e32 v6, 4, v0
	s_add_u32 s4, s10, s6
	v_lshl_add_u64 v[4:5], s[24:25], 0, v[2:3]
	v_and_b32_e32 v6, 0x70, v6
	v_mov_b32_e32 v7, v3
	v_lshlrev_b32_e32 v56, 4, v0
	v_mov_b32_e32 v57, v3
	s_addc_u32 s5, s11, s7
	v_lshl_add_u64 v[4:5], v[4:5], 0, v[6:7]
	s_mov_b64 s[46:47], 0x4000
	v_lshl_add_u64 v[250:251], v[4:5], 0, s[46:47]
	s_movk_i32 s8, 0x2000
	v_lshl_add_u64 v[6:7], s[4:5], 0, v[56:57]
	global_load_dwordx4 v[8:11], v[4:5], off sc1 nt
	global_load_dwordx4 v[12:15], v[250:251], off sc1 nt
	global_load_dwordx4 v[16:19], v56, s[4:5] sc1
	v_add_co_u32_e64 v28, s[4:5], s8, v6
	s_mov_b32 s33, 0xa000
	s_nop 0
	v_addc_co_u32_e64 v29, s[4:5], 0, v7, s[4:5]
	s_movk_i32 s4, 0x4000
	s_nop 0
	v_add_co_u32_e64 v30, s[4:5], s4, v6
	s_mov_b32 s6, 0xe000
	s_nop 0
	v_addc_co_u32_e64 v31, s[4:5], 0, v7, s[4:5]
	global_load_dwordx4 v[20:23], v[28:29], off sc1
	global_load_dwordx4 v[24:27], v[30:31], off sc1
	s_movk_i32 s4, 0x6000
	v_add_co_u32_e64 v40, s[4:5], s4, v6
	v_lshlrev_b32_e32 v57, 6, v1
	s_nop 0
	v_addc_co_u32_e64 v41, s[4:5], 0, v7, s[4:5]
	global_load_dwordx4 v[28:31], v[40:41], off sc1
	global_load_dwordx4 v[32:35], v[4:5], off offset:128 sc1 nt
	global_load_dwordx4 v[36:39], v[250:251], off offset:128 sc1 nt
	s_mov_b32 s4, 0x8000
	v_add_co_u32_e64 v40, s[4:5], s4, v6
	v_bitop3_b32 v58, v56, 48, v0 bitop3:0x48
	s_nop 0
	v_addc_co_u32_e64 v41, s[4:5], 0, v7, s[4:5]
	v_add_co_u32_e64 v44, s[4:5], s33, v6
	global_load_dwordx4 v[40:43], v[40:41], off sc1
	s_nop 0
	v_addc_co_u32_e64 v45, s[4:5], 0, v7, s[4:5]
	s_mov_b32 s4, 0xc000
	s_nop 0
	v_add_co_u32_e64 v48, s[4:5], s4, v6
	global_load_dwordx4 v[44:47], v[44:45], off sc1
	s_nop 0
	v_addc_co_u32_e64 v49, s[4:5], 0, v7, s[4:5]
	v_add_co_u32_e64 v52, s[4:5], s6, v6
	global_load_dwordx4 v[48:51], v[48:49], off sc1
	s_nop 0
	v_addc_co_u32_e64 v53, s[4:5], 0, v7, s[4:5]
	global_load_dwordx4 v[52:55], v[52:53], off sc1
	s_mov_b32 s4, 0x1e000
	v_bfe_u32 v57, v0, 1, 2
	v_bfe_u32 v58, v254, 2, 2
	v_xor_b32_e32 v57, v57, v58
	v_lshlrev_b32_e32 v57, 4, v57
	v_and_b32_e32 v58, 1, v0
	v_lshl_or_b32 v57, v58, 3, v57
	v_lshl_add_u32 v209, v254, 6, v57
	v_xor_b32_e32 v248, 32, v209
	v_add_u32_e32 v248, 0x200, v248
	v_add_u32_e32 v208, 0, v56
	v_readfirstlane_b32 s30, v0
	v_bfe_u32 v207, v0, 5, 1
	v_bitop3_b32 v1, v207, v1, 3 bitop3:0x78
	v_lshlrev_b32_e32 v210, 4, v1
	s_mov_b32 s34, 0x14000
	v_add_u32_e32 v213, 0x2000, v208
	s_mov_b32 s43, 0
	s_lshr_b32 s29, s30, 6
	s_mov_b32 s35, -2
	s_mov_b32 s36, 0xffff2000
	s_mov_b32 s37, 0xffff4000
	s_mov_b32 s38, 0xffff6000
	s_movk_i32 s39, 0x8000
	s_movk_i32 s40, 0xa000
	s_movk_i32 s41, 0xc000
	s_movk_i32 s42, 0xe000
	s_mov_b64 s[26:27], 0x100
	v_mov_b32_e32 v56, v3
	v_mov_b32_e32 v57, v3
	v_mov_b32_e32 v58, v3
	v_mov_b32_e32 v59, v3
	v_mov_b32_e32 v60, v3
	v_mov_b32_e32 v61, v3
	v_mov_b32_e32 v62, v3
	v_mov_b32_e32 v63, v3
	v_mov_b32_e32 v64, v3
	v_mov_b32_e32 v65, v3
	v_mov_b32_e32 v66, v3
	v_mov_b32_e32 v67, v3
	v_mov_b32_e32 v68, v3
	v_mov_b32_e32 v69, v3
	v_mov_b32_e32 v70, v3
	s_waitcnt vmcnt(11)
	v_cvt_pk_f16_f32 v8, v8, v9
	v_cvt_pk_f16_f32 v9, v10, v11
	s_waitcnt vmcnt(10)
	v_cvt_pk_f16_f32 v10, v12, v13
	v_cvt_pk_f16_f32 v11, v14, v15
	ds_write_b64 v209, v[8:9]
	ds_write_b64 v248, v[10:11]
	v_and_b32_e32 v10, 31, v0
	s_waitcnt vmcnt(9)
	ds_write_b128 v208, v[16:19] offset:8192
	s_waitcnt vmcnt(8)
	ds_write_b128 v208, v[20:23] offset:16384
	s_waitcnt vmcnt(7)
	ds_write_b128 v208, v[24:27] offset:24576
	s_load_dwordx2 s[16:17], s[0:1], 0x50
	s_load_dwordx4 s[12:15], s[0:1], 0x40
	s_load_dwordx8 s[4:11], s[0:1], 0x20
	s_lshl_b32 s0, s30, 1
	s_and_b32 s31, s0, 0x180
	s_lshr_b32 s0, s30, 2
	v_bfe_u32 v11, v0, 2, 2
	s_and_b32 s0, s0, 0x3fffffc0
	s_waitcnt vmcnt(5)
	v_cvt_pk_f16_f32 v8, v32, v33
	v_cvt_pk_f16_f32 v9, v34, v35
	v_or_b32_e32 v12, s31, v10
	v_or_b32_e32 v206, s0, v10
	v_bitop3_b32 v1, v207, v11, 2 bitop3:0x36
	s_waitcnt vmcnt(4)
	v_cvt_pk_f16_f32 v10, v36, v37
	v_cvt_pk_f16_f32 v11, v38, v39
	s_mov_b32 s0, 0x10000
	ds_write_b128 v208, v[28:31] offset:32768
	ds_write_b64 v209, v[8:9] offset:40960
	ds_write_b64 v248, v[10:11] offset:40960
	v_add_co_u32_e64 v8, s[0:1], s0, v6
	global_load_dwordx4 v[154:157], v[250:251], off offset:256 sc1 nt
	global_load_dwordx4 v[162:165], v[4:5], off offset:256 sc1 nt
	v_addc_co_u32_e64 v9, s[0:1], 0, v7, s[0:1]
	s_mov_b32 s0, 0x12000
	global_load_dwordx4 v[158:161], v[8:9], off sc1
	v_add_co_u32_e64 v8, s[0:1], s0, v6
	v_lshl_add_u32 v211, v12, 6, 0
	s_nop 0
	v_addc_co_u32_e64 v9, s[0:1], 0, v7, s[0:1]
	v_add_co_u32_e64 v10, s[0:1], s34, v6
	v_add_u32_e32 v14, 0x12000, v208
	s_nop 0
	v_addc_co_u32_e64 v11, s[0:1], 0, v7, s[0:1]
	s_mov_b32 s0, 0x16000
	s_nop 0
	v_add_co_u32_e64 v12, s[0:1], s0, v6
	s_waitcnt vmcnt(3)
	ds_write_b128 v14, v[52:55]
	v_addc_co_u32_e64 v13, s[0:1], 0, v7, s[0:1]
	s_mov_b32 s0, 0x18000
	s_nop 0
	v_add_co_u32_e64 v14, s[0:1], s0, v6
	ds_write_b128 v208, v[40:43] offset:49152
	s_nop 0
	v_addc_co_u32_e64 v15, s[0:1], 0, v7, s[0:1]
	s_mov_b32 s0, 0x1a000
	s_nop 0
	v_add_co_u32_e64 v16, s[0:1], s0, v6
	ds_write_b128 v208, v[44:47] offset:57344
	s_nop 0
	v_addc_co_u32_e64 v17, s[0:1], 0, v7, s[0:1]
	s_mov_b32 s0, 0x1c000
	ds_write_b128 v213, v[48:51] offset:57344
	v_add_co_u32_e64 v18, s[0:1], s0, v6
	v_add_u32_e32 v216, v211, v210
	s_nop 0
	v_addc_co_u32_e64 v19, s[0:1], 0, v7, s[0:1]
	global_load_dwordx4 v[174:177], v[8:9], off sc1
	global_load_dwordx4 v[166:169], v[10:11], off sc1
	global_load_dwordx4 v[170:173], v[12:13], off sc1
	global_load_dwordx4 v[142:145], v[250:251], off offset:384 sc1 nt
	global_load_dwordx4 v[150:153], v[4:5], off offset:384 sc1 nt
	global_load_dwordx4 v[138:141], v[14:15], off sc1
	global_load_dwordx4 v[146:149], v[16:17], off sc1
	global_load_dwordx4 v[134:137], v[18:19], off sc1
	s_mov_b32 s0, 0x1e000
	v_add_co_u32_e64 v8, s[0:1], s0, v6
	s_nop 1
	v_addc_co_u32_e64 v9, s[0:1], 0, v7, s[0:1]
	global_load_dwordx4 v[130:133], v[8:9], off sc1
	s_waitcnt lgkmcnt(0)
	s_barrier
	v_lshl_add_u32 v218, v206, 6, 0
	v_add_u32_e32 v217, v218, v210
	ds_read_b128 v[198:201], v216 offset:8192
	ds_read_b128 v[194:197], v216 offset:10240
	ds_read_b128 v[190:193], v216 offset:12288
	ds_read_b128 v[178:181], v216 offset:14336
	ds_read_b128 v[186:189], v217
	ds_read_b128 v[182:185], v217 offset:2048
	v_and_b32_e32 v20, 7, v0
	v_lshl_or_b32 v2, v20, 4, v2
	s_mov_b64 s[0:1], 0x2e000
	v_lshlrev_b32_e32 v212, 4, v1
	v_lshl_add_u64 v[202:203], v[6:7], 0, s[0:1]
	s_mov_b64 s[0:1], 0x290
	v_lshl_add_u64 v[4:5], s[24:25], 0, v[2:3]
	v_lshl_add_u64 v[204:205], v[4:5], 0, s[0:1]
	v_lshl_add_u64 v[252:253], v[204:205], 0, s[46:47]
	s_mov_b64 s[24:25], 0x10000
	v_mov_b32_e32 v2, v3
	v_mov_b32_e32 v4, v3
	v_mov_b32_e32 v5, v3
	v_mov_b32_e32 v6, v3
	v_mov_b32_e32 v7, v3
	v_mov_b32_e32 v8, v3
	v_mov_b32_e32 v9, v3
	v_mov_b32_e32 v10, v3
	v_mov_b32_e32 v11, v3
	v_mov_b32_e32 v12, v3
	v_mov_b32_e32 v13, v3
	v_mov_b32_e32 v14, v3
	v_mov_b32_e32 v15, v3
	v_mov_b32_e32 v16, v3
	v_mov_b32_e32 v17, v3
	v_mov_b32_e32 v18, v3
	v_mov_b32_e32 v19, v3
	v_mov_b32_e32 v20, v3
	v_mov_b32_e32 v21, v3
	v_mov_b32_e32 v22, v3
	v_mov_b32_e32 v23, v3
	v_mov_b32_e32 v24, v3
	v_mov_b32_e32 v25, v3
	v_mov_b32_e32 v26, v3
	v_mov_b32_e32 v27, v3
	v_mov_b32_e32 v28, v3
	v_mov_b32_e32 v29, v3
	v_mov_b32_e32 v30, v3
	v_mov_b32_e32 v31, v3
	v_mov_b32_e32 v32, v3
	v_mov_b32_e32 v33, v3
	v_mov_b32_e32 v34, v3
	v_mov_b32_e32 v35, v3
	v_mov_b32_e32 v36, v3
	v_mov_b32_e32 v37, v3
	v_mov_b32_e32 v38, v3
	v_mov_b32_e32 v39, v3
	v_mov_b32_e32 v40, v3
	v_mov_b32_e32 v41, v3
	v_mov_b32_e32 v42, v3
	v_mov_b32_e32 v43, v3
	v_mov_b32_e32 v44, v3
	v_mov_b32_e32 v45, v3
	v_mov_b32_e32 v46, v3
	v_mov_b32_e32 v47, v3
	v_mov_b32_e32 v48, v3
	v_mov_b32_e32 v49, v3
	v_mov_b32_e32 v50, v3
	v_mov_b32_e32 v51, v3
	v_mov_b32_e32 v52, v3
	v_mov_b32_e32 v53, v3
	v_mov_b32_e32 v54, v3
	v_mov_b32_e32 v55, v3
	v_mov_b32_e32 v71, v3
	v_mov_b32_e32 v72, v3
	v_mov_b32_e32 v73, v3
	v_mov_b32_e32 v74, v3
	v_mov_b32_e32 v75, v3
	v_mov_b32_e32 v76, v3
	v_mov_b32_e32 v77, v3
	v_mov_b32_e32 v78, v3
	v_mov_b32_e32 v79, v3
	v_mov_b32_e32 v80, v3
	v_mov_b32_e32 v81, v3
	v_mov_b32_e32 v82, v3
	v_mov_b32_e32 v83, v3
	v_mov_b32_e32 v84, v3
	v_mov_b32_e32 v85, v3
	v_mov_b32_e32 v86, v3
	v_mov_b32_e32 v87, v3
	v_mov_b32_e32 v88, v3
	v_mov_b32_e32 v89, v3
	v_mov_b32_e32 v90, v3
	v_mov_b32_e32 v91, v3
	v_mov_b32_e32 v92, v3
	v_mov_b32_e32 v93, v3
	v_mov_b32_e32 v94, v3
	v_mov_b32_e32 v95, v3
	v_mov_b32_e32 v96, v3
	v_mov_b32_e32 v97, v3
	v_mov_b32_e32 v98, v3
	v_mov_b32_e32 v99, v3
	v_mov_b32_e32 v100, v3
	v_mov_b32_e32 v101, v3
	v_mov_b32_e32 v102, v3
	v_mov_b32_e32 v103, v3
	v_mov_b32_e32 v104, v3
	v_mov_b32_e32 v105, v3
	v_mov_b32_e32 v106, v3
	v_mov_b32_e32 v107, v3
	v_mov_b32_e32 v108, v3
	v_mov_b32_e32 v109, v3
	v_mov_b32_e32 v110, v3
	v_mov_b32_e32 v111, v3
	v_mov_b32_e32 v112, v3
	v_mov_b32_e32 v113, v3
	v_mov_b32_e32 v114, v3
	v_mov_b32_e32 v115, v3
	v_mov_b32_e32 v116, v3
	v_mov_b32_e32 v117, v3
	v_mov_b32_e32 v118, v3
	v_mov_b32_e32 v119, v3
	v_mov_b32_e32 v120, v3
	v_mov_b32_e32 v121, v3
	v_mov_b32_e32 v122, v3
	v_mov_b32_e32 v123, v3
	v_mov_b32_e32 v124, v3
	v_mov_b32_e32 v125, v3
	v_mov_b32_e32 v126, v3
	v_mov_b32_e32 v127, v3
	v_mov_b32_e32 v128, v3
	v_mov_b32_e32 v129, v3
	v_and_b32_e32 v1, 63, v0
	v_add_u32_e32 v215, v211, v212
	v_add_u32_e32 v214, v218, v212
	s_cmp_ge_u32 s29, 4
	s_cbranch_scc0 .Lproj_prio_done
	s_setprio 1
.Lproj_prio_done:
.LBB1_1:
	s_waitcnt lgkmcnt(0)
	v_mfma_f32_32x32x16_f16 v[114:129], v[198:201], v[186:189], v[114:129]
	s_mov_b32 s44, s33
	s_mov_b32 s33, s43
	v_mfma_f32_32x32x16_f16 v[98:113], v[198:201], v[182:185], v[98:113]
	v_add_u32_e32 v219, s33, v215
	ds_read_b128 v[198:201], v219 offset:8192
	ds_read_b128 v[220:223], v219 offset:10240
	ds_read_b128 v[224:227], v219 offset:12288
	ds_read_b128 v[228:231], v219 offset:14336
	v_add_u32_e32 v219, s33, v214
	ds_read_b128 v[232:235], v219
	ds_read_b128 v[236:239], v219 offset:2048
	s_waitcnt vmcnt(10)
	v_cvt_pk_f16_f32 v162, v162, v163
	v_cvt_pk_f16_f32 v163, v164, v165
	v_cvt_pk_f16_f32 v164, v154, v155
	v_cvt_pk_f16_f32 v165, v156, v157
	v_add_u32_e32 v154, s34, v209
	ds_write_b64 v154, v[162:163]
	v_add_u32_e32 v154, s34, v248
	ds_write_b64 v154, v[164:165]
	v_mfma_f32_32x32x16_f16 v[82:97], v[194:197], v[186:189], v[82:97]
	v_add_u32_e32 v154, s34, v208
	s_waitcnt vmcnt(9)
	ds_write_b128 v154, v[158:161] offset:8192
	s_waitcnt vmcnt(8)
	ds_write_b128 v154, v[174:177] offset:16384
	v_mfma_f32_32x32x16_f16 v[66:81], v[194:197], v[182:185], v[66:81]
	v_mfma_f32_32x32x16_f16 v[50:65], v[190:193], v[186:189], v[50:65]
	s_waitcnt vmcnt(7)
	ds_write_b128 v154, v[166:169] offset:24576
	s_waitcnt vmcnt(6)
	ds_write_b128 v154, v[170:173] offset:32768
	v_mfma_f32_32x32x16_f16 v[34:49], v[190:193], v[182:185], v[34:49]
	v_add_co_u32_e64 v158, s[0:1], s36, v202
	global_load_dwordx4 v[154:157], v[252:253], off offset:-144 sc1 nt
	global_load_dwordx4 v[162:165], v[204:205], off offset:-144 sc1 nt
	v_addc_co_u32_e64 v159, s[0:1], -1, v203, s[0:1]
	v_add_co_u32_e64 v166, s[0:1], s37, v202
	v_mfma_f32_32x32x16_f16 v[18:33], v[178:181], v[186:189], v[18:33]
	s_nop 0
	v_addc_co_u32_e64 v167, s[0:1], -1, v203, s[0:1]
	global_load_dwordx4 v[158:161], v[158:159], off sc1
	s_nop 0
	global_load_dwordx4 v[174:177], v[166:167], off sc1
	v_add_co_u32_e64 v166, s[0:1], s38, v202
	s_nop 1
	v_addc_co_u32_e64 v167, s[0:1], -1, v203, s[0:1]
	v_add_co_u32_e64 v170, s[0:1], s39, v202
	v_mfma_f32_32x32x16_f16 v[2:17], v[178:181], v[182:185], v[2:17]
	s_nop 0
	v_addc_co_u32_e64 v171, s[0:1], -1, v203, s[0:1]
	global_load_dwordx4 v[166:169], v[166:167], off sc1
	s_nop 0
	global_load_dwordx4 v[170:173], v[170:171], off sc1
	v_add_u32_e32 v190, s44, v216
	ds_read_b128 v[178:181], v190 offset:8192
	ds_read_b128 v[182:185], v190 offset:10240
	ds_read_b128 v[186:189], v190 offset:12288
	ds_read_b128 v[190:193], v190 offset:14336
	v_add_u32_e32 v219, s44, v217
	ds_read_b128 v[194:197], v219
	ds_read_b128 v[240:243], v219 offset:2048
	s_waitcnt lgkmcnt(12)
	v_mfma_f32_32x32x16_f16 v[114:129], v[198:201], v[232:235], v[114:129]
	s_waitcnt lgkmcnt(11)
	v_mfma_f32_32x32x16_f16 v[98:113], v[198:201], v[236:239], v[98:113]
	v_mfma_f32_32x32x16_f16 v[82:97], v[220:223], v[232:235], v[82:97]
	v_mfma_f32_32x32x16_f16 v[66:81], v[220:223], v[236:239], v[66:81]
	v_mfma_f32_32x32x16_f16 v[50:65], v[224:227], v[232:235], v[50:65]
	v_mfma_f32_32x32x16_f16 v[34:49], v[224:227], v[236:239], v[34:49]
	v_mfma_f32_32x32x16_f16 v[18:33], v[228:231], v[232:235], v[18:33]
	v_mfma_f32_32x32x16_f16 v[2:17], v[228:231], v[236:239], v[2:17]
	s_waitcnt lgkmcnt(1)
	v_mfma_f32_32x32x16_f16 v[114:129], v[178:181], v[194:197], v[114:129]
	s_waitcnt lgkmcnt(0)
	s_barrier
	s_waitcnt lgkmcnt(0)
	v_mfma_f32_32x32x16_f16 v[98:113], v[178:181], v[240:243], v[98:113]
	v_add_u32_e32 v178, s44, v215
	ds_read_b128 v[220:223], v178 offset:8192
	ds_read_b128 v[224:227], v178 offset:10240
	ds_read_b128 v[228:231], v178 offset:12288
	ds_read_b128 v[232:235], v178 offset:14336
	v_add_u32_e32 v178, s44, v214
	ds_read_b128 v[236:239], v178
	ds_read_b128 v[244:247], v178 offset:2048
	s_waitcnt vmcnt(10)
	v_cvt_pk_f16_f32 v150, v150, v151
	v_cvt_pk_f16_f32 v151, v152, v153
	v_cvt_pk_f16_f32 v152, v142, v143
	v_cvt_pk_f16_f32 v153, v144, v145
	v_add_u32_e32 v142, s33, v209
	ds_write_b64 v142, v[150:151]
	v_add_u32_e32 v142, s33, v248
	ds_write_b64 v142, v[152:153]
	v_mfma_f32_32x32x16_f16 v[82:97], v[182:185], v[194:197], v[82:97]
	v_add_u32_e32 v142, s33, v208
	s_waitcnt vmcnt(9)
	ds_write_b128 v142, v[138:141] offset:8192
	s_waitcnt vmcnt(8)
	ds_write_b128 v142, v[146:149] offset:16384
	v_mfma_f32_32x32x16_f16 v[66:81], v[182:185], v[240:243], v[66:81]
	v_mfma_f32_32x32x16_f16 v[50:65], v[186:189], v[194:197], v[50:65]
	s_waitcnt vmcnt(7)
	ds_write_b128 v142, v[134:137] offset:24576
	s_waitcnt vmcnt(6)
	ds_write_b128 v142, v[130:133] offset:32768
	v_mfma_f32_32x32x16_f16 v[34:49], v[186:189], v[240:243], v[34:49]
	v_add_co_u32_e64 v130, s[0:1], s40, v202
	global_load_dwordx4 v[142:145], v[252:253], off offset:-16 sc1 nt
	global_load_dwordx4 v[150:153], v[204:205], off offset:-16 sc1 nt
	v_addc_co_u32_e64 v131, s[0:1], -1, v203, s[0:1]
	v_add_co_u32_e64 v132, s[0:1], s41, v202
	v_mfma_f32_32x32x16_f16 v[18:33], v[190:193], v[194:197], v[18:33]
	s_nop 0
	v_addc_co_u32_e64 v133, s[0:1], -1, v203, s[0:1]
	global_load_dwordx4 v[138:141], v[130:131], off sc1
	global_load_dwordx4 v[146:149], v[132:133], off sc1
	v_add_co_u32_e64 v130, s[0:1], s42, v202
	s_nop 1
	v_addc_co_u32_e64 v131, s[0:1], -1, v203, s[0:1]
	global_load_dwordx4 v[134:137], v[130:131], off sc1
	s_nop 0
	global_load_dwordx4 v[130:133], v[202:203], off sc1
	v_mfma_f32_32x32x16_f16 v[2:17], v[190:193], v[240:243], v[2:17]
	v_add_u32_e32 v178, s34, v216
	ds_read_b128 v[198:201], v178 offset:8192
	ds_read_b128 v[194:197], v178 offset:10240
	ds_read_b128 v[190:193], v178 offset:12288
	ds_read_b128 v[178:181], v178 offset:14336
	v_add_u32_e32 v182, s34, v217
	ds_read_b128 v[186:189], v182
	ds_read_b128 v[182:185], v182 offset:2048
	s_waitcnt lgkmcnt(12)
	v_mfma_f32_32x32x16_f16 v[114:129], v[220:223], v[236:239], v[114:129]
	s_waitcnt lgkmcnt(11)
	v_mfma_f32_32x32x16_f16 v[98:113], v[220:223], v[244:247], v[98:113]
	v_mfma_f32_32x32x16_f16 v[82:97], v[224:227], v[236:239], v[82:97]
	v_mfma_f32_32x32x16_f16 v[66:81], v[224:227], v[244:247], v[66:81]
	v_mfma_f32_32x32x16_f16 v[50:65], v[228:231], v[236:239], v[50:65]
	v_mfma_f32_32x32x16_f16 v[34:49], v[228:231], v[244:247], v[34:49]
	v_mfma_f32_32x32x16_f16 v[18:33], v[232:235], v[236:239], v[18:33]
	v_mfma_f32_32x32x16_f16 v[2:17], v[232:235], v[244:247], v[2:17]
	s_waitcnt lgkmcnt(0)
	s_barrier
	s_add_i32 s35, s35, 2
	v_lshl_add_u64 v[202:203], v[202:203], 0, s[24:25]
	v_lshl_add_u64 v[204:205], v[204:205], 0, s[26:27]
	v_lshl_add_u64 v[252:253], v[252:253], 0, s[26:27]
	s_mov_b32 s43, s34
	s_cmp_gt_u32 s35, 9
	s_mov_b32 s34, s44
	s_cbranch_scc0 .LBB1_1
	s_and_b64 s[0:1], s[20:21], exec
	s_cselect_b32 s6, s6, s8
	s_cselect_b32 s7, s7, s9
	s_and_b64 s[0:1], vcc, exec
	s_cselect_b32 s1, s5, s7
	s_cselect_b32 s0, s4, s6
	v_mov_b32_e32 v202, 0x3e38aa3b
	s_waitcnt lgkmcnt(1)
	v_mfma_f32_32x32x16_f16 v[114:129], v[198:201], v[186:189], v[114:129]
	v_cndmask_b32_e32 v202, 1.0, v202, vcc
	s_waitcnt lgkmcnt(0)
	v_mfma_f32_32x32x16_f16 v[98:113], v[198:201], v[182:185], v[98:113]
	ds_read_b128 v[198:201], v215 offset:8192
	ds_read_b128 v[220:223], v215 offset:10240
	ds_read_b128 v[224:227], v215 offset:12288
	ds_read_b128 v[228:231], v215 offset:14336
	ds_read_b128 v[232:235], v214
	ds_read_b128 v[236:239], v214 offset:2048
	s_waitcnt vmcnt(10)
	v_cvt_pk_f16_f32 v162, v162, v163
	v_cvt_pk_f16_f32 v163, v164, v165
	v_cvt_pk_f16_f32 v164, v154, v155
	v_cvt_pk_f16_f32 v165, v156, v157
	v_add_u32_e32 v154, 0x14000, v209
	ds_write_b64 v154, v[162:163]
	v_add_u32_e32 v154, 0x14000, v248
	ds_write_b64 v154, v[164:165]
	v_add_u32_e32 v154, 0x14000, v213
	s_waitcnt vmcnt(9)
	ds_write_b128 v154, v[158:161]
	v_add_u32_e32 v154, 0x16000, v213
	v_mfma_f32_32x32x16_f16 v[82:97], v[194:197], v[186:189], v[82:97]
	s_waitcnt vmcnt(8)
	ds_write_b128 v154, v[174:177]
	v_mfma_f32_32x32x16_f16 v[66:81], v[194:197], v[182:185], v[66:81]
	v_add_u32_e32 v154, 0x18000, v213
	s_waitcnt vmcnt(7)
	ds_write_b128 v154, v[166:169]
	v_add_u32_e32 v154, 0x1a000, v213
	v_mfma_f32_32x32x16_f16 v[50:65], v[190:193], v[186:189], v[50:65]
	s_waitcnt vmcnt(6)
	ds_write_b128 v154, v[170:173]
	v_mfma_f32_32x32x16_f16 v[34:49], v[190:193], v[182:185], v[34:49]
	v_mfma_f32_32x32x16_f16 v[18:33], v[178:181], v[186:189], v[18:33]
	v_mfma_f32_32x32x16_f16 v[2:17], v[178:181], v[182:185], v[2:17]
	ds_read_b128 v[154:157], v216 offset:49152
	ds_read_b128 v[158:161], v216 offset:51200
	ds_read_b128 v[162:165], v216 offset:53248
	ds_read_b128 v[166:169], v216 offset:55296
	ds_read_b128 v[170:173], v217 offset:40960
	ds_read_b128 v[174:177], v217 offset:43008
	s_waitcnt lgkmcnt(12)
	v_mfma_f32_32x32x16_f16 v[114:129], v[198:201], v[232:235], v[114:129]
	s_waitcnt lgkmcnt(11)
	v_mfma_f32_32x32x16_f16 v[98:113], v[198:201], v[236:239], v[98:113]
	v_mfma_f32_32x32x16_f16 v[82:97], v[220:223], v[232:235], v[82:97]
	v_mfma_f32_32x32x16_f16 v[66:81], v[220:223], v[236:239], v[66:81]
	v_mfma_f32_32x32x16_f16 v[50:65], v[224:227], v[232:235], v[50:65]
	v_mfma_f32_32x32x16_f16 v[34:49], v[224:227], v[236:239], v[34:49]
	v_mfma_f32_32x32x16_f16 v[18:33], v[228:231], v[232:235], v[18:33]
	v_mfma_f32_32x32x16_f16 v[2:17], v[228:231], v[236:239], v[2:17]
	s_waitcnt lgkmcnt(0)
	s_barrier
	s_waitcnt lgkmcnt(1)
	v_mfma_f32_32x32x16_f16 v[114:129], v[154:157], v[170:173], v[114:129]
	s_waitcnt lgkmcnt(0)
	v_mfma_f32_32x32x16_f16 v[98:113], v[154:157], v[174:177], v[98:113]
	ds_read_b128 v[154:157], v215 offset:49152
	ds_read_b128 v[178:181], v215 offset:51200
	ds_read_b128 v[182:185], v215 offset:53248
	ds_read_b128 v[186:189], v215 offset:55296
	ds_read_b128 v[190:193], v214 offset:40960
	ds_read_b128 v[194:197], v214 offset:43008
	s_waitcnt vmcnt(4)
	v_cvt_pk_f16_f32 v150, v150, v151
	v_cvt_pk_f16_f32 v151, v152, v153
	v_cvt_pk_f16_f32 v152, v142, v143
	v_cvt_pk_f16_f32 v153, v144, v145
	ds_write_b64 v209, v[150:151]
	ds_write_b64 v248, v[152:153]
	v_mfma_f32_32x32x16_f16 v[82:97], v[158:161], v[170:173], v[82:97]
	s_waitcnt vmcnt(3)
	ds_write_b128 v208, v[138:141] offset:8192
	s_waitcnt vmcnt(2)
	ds_write_b128 v208, v[146:149] offset:16384
	v_mfma_f32_32x32x16_f16 v[66:81], v[158:161], v[174:177], v[66:81]
	v_mfma_f32_32x32x16_f16 v[50:65], v[162:165], v[170:173], v[50:65]
	s_waitcnt vmcnt(1)
	ds_write_b128 v208, v[134:137] offset:24576
	s_waitcnt vmcnt(0)
	ds_write_b128 v208, v[130:133] offset:32768
	v_mfma_f32_32x32x16_f16 v[34:49], v[162:165], v[174:177], v[34:49]
	v_mfma_f32_32x32x16_f16 v[18:33], v[166:169], v[170:173], v[18:33]
	v_mfma_f32_32x32x16_f16 v[2:17], v[166:169], v[174:177], v[2:17]
	v_add_u32_e32 v158, 0x16000, v211
	v_add_u32_e32 v142, v158, v210
	ds_read_b128 v[130:133], v142
	ds_read_b128 v[134:137], v142 offset:2048
	ds_read_b128 v[138:141], v142 offset:4096
	ds_read_b128 v[142:145], v142 offset:6144
	v_add_u32_e32 v166, 0x14000, v218
	v_add_u32_e32 v150, v166, v210
	ds_read_b128 v[146:149], v150
	ds_read_b128 v[150:153], v150 offset:2048
	s_waitcnt lgkmcnt(12)
	v_mfma_f32_32x32x16_f16 v[114:129], v[154:157], v[190:193], v[114:129]
	s_waitcnt lgkmcnt(11)
	v_mfma_f32_32x32x16_f16 v[98:113], v[154:157], v[194:197], v[98:113]
	v_mfma_f32_32x32x16_f16 v[82:97], v[178:181], v[190:193], v[82:97]
	v_mfma_f32_32x32x16_f16 v[66:81], v[178:181], v[194:197], v[66:81]
	v_mfma_f32_32x32x16_f16 v[50:65], v[182:185], v[190:193], v[50:65]
	v_mfma_f32_32x32x16_f16 v[34:49], v[182:185], v[194:197], v[34:49]
	v_mfma_f32_32x32x16_f16 v[18:33], v[186:189], v[190:193], v[18:33]
	v_mfma_f32_32x32x16_f16 v[2:17], v[186:189], v[194:197], v[2:17]
	s_waitcnt lgkmcnt(0)
	s_barrier
	s_waitcnt lgkmcnt(1)
	v_mfma_f32_32x32x16_f16 v[114:129], v[130:133], v[146:149], v[114:129]
	s_waitcnt lgkmcnt(0)
	v_mfma_f32_32x32x16_f16 v[98:113], v[130:133], v[150:153], v[98:113]
	v_add_u32_e32 v162, v158, v212
	ds_read_b128 v[130:133], v162
	ds_read_b128 v[154:157], v162 offset:2048
	ds_read_b128 v[158:161], v162 offset:4096
	ds_read_b128 v[162:165], v162 offset:6144
	v_add_u32_e32 v170, v166, v212
	ds_read_b128 v[166:169], v170
	ds_read_b128 v[170:173], v170 offset:2048
	v_mfma_f32_32x32x16_f16 v[82:97], v[134:137], v[146:149], v[82:97]
	v_mfma_f32_32x32x16_f16 v[66:81], v[134:137], v[150:153], v[66:81]
	v_mfma_f32_32x32x16_f16 v[50:65], v[138:141], v[146:149], v[50:65]
	v_mfma_f32_32x32x16_f16 v[34:49], v[138:141], v[150:153], v[34:49]
	v_mfma_f32_32x32x16_f16 v[18:33], v[142:145], v[146:149], v[18:33]
	v_mfma_f32_32x32x16_f16 v[2:17], v[142:145], v[150:153], v[2:17]
	ds_read_b128 v[134:137], v216 offset:8192
	ds_read_b128 v[138:141], v216 offset:10240
	ds_read_b128 v[142:145], v216 offset:12288
	ds_read_b128 v[146:149], v216 offset:14336
	ds_read_b128 v[150:153], v217
	ds_read_b128 v[174:177], v217 offset:2048
	s_waitcnt lgkmcnt(7)
	v_mfma_f32_32x32x16_f16 v[114:129], v[130:133], v[166:169], v[114:129]
	s_waitcnt lgkmcnt(6)
	v_mfma_f32_32x32x16_f16 v[98:113], v[130:133], v[170:173], v[98:113]
	v_mfma_f32_32x32x16_f16 v[82:97], v[154:157], v[166:169], v[82:97]
	v_mfma_f32_32x32x16_f16 v[66:81], v[154:157], v[170:173], v[66:81]
	v_mfma_f32_32x32x16_f16 v[50:65], v[158:161], v[166:169], v[50:65]
	v_mfma_f32_32x32x16_f16 v[34:49], v[158:161], v[170:173], v[34:49]
	v_mfma_f32_32x32x16_f16 v[18:33], v[162:165], v[166:169], v[18:33]
	v_mfma_f32_32x32x16_f16 v[2:17], v[162:165], v[170:173], v[2:17]
	s_waitcnt lgkmcnt(0)
	s_barrier
	s_waitcnt lgkmcnt(1)
	v_mfma_f32_32x32x16_f16 v[114:129], v[134:137], v[150:153], v[114:129]
	s_waitcnt lgkmcnt(0)
	v_mfma_f32_32x32x16_f16 v[98:113], v[134:137], v[174:177], v[98:113]
	ds_read_b128 v[130:133], v215 offset:8192
	ds_read_b128 v[134:137], v215 offset:10240
	ds_read_b128 v[154:157], v215 offset:12288
	ds_read_b128 v[158:161], v215 offset:14336
	ds_read_b128 v[162:165], v214
	ds_read_b128 v[166:169], v214 offset:2048
	v_mfma_f32_32x32x16_f16 v[82:97], v[138:141], v[150:153], v[82:97]
	v_mfma_f32_32x32x16_f16 v[66:81], v[138:141], v[174:177], v[66:81]
	v_mfma_f32_32x32x16_f16 v[50:65], v[142:145], v[150:153], v[50:65]
	v_mfma_f32_32x32x16_f16 v[34:49], v[142:145], v[174:177], v[34:49]
	v_mfma_f32_32x32x16_f16 v[18:33], v[146:149], v[150:153], v[18:33]
	v_mfma_f32_32x32x16_f16 v[2:17], v[146:149], v[174:177], v[2:17]
	s_waitcnt lgkmcnt(1)
	v_mfma_f32_32x32x16_f16 v[114:129], v[130:133], v[162:165], v[114:129]
	s_waitcnt lgkmcnt(0)
	v_mfma_f32_32x32x16_f16 v[98:113], v[130:133], v[166:169], v[98:113]
	v_mfma_f32_32x32x16_f16 v[82:97], v[134:137], v[162:165], v[82:97]
	v_mfma_f32_32x32x16_f16 v[66:81], v[134:137], v[166:169], v[66:81]
	v_mfma_f32_32x32x16_f16 v[50:65], v[154:157], v[162:165], v[50:65]
	v_mfma_f32_32x32x16_f16 v[34:49], v[154:157], v[166:169], v[34:49]
	v_mfma_f32_32x32x16_f16 v[18:33], v[158:161], v[162:165], v[18:33]
	v_mfma_f32_32x32x16_f16 v[2:17], v[158:161], v[166:169], v[2:17]
	v_lshl_or_b32 v130, v207, 2, s31
	s_waitcnt lgkmcnt(0)
	s_barrier
	s_cbranch_vccnz .Lepi_q
	v_lshlrev_b32_e32 v154, 2, v130
	global_load_dwordx4 v[134:137], v154, s[0:1]
	global_load_dwordx4 v[150:153], v154, s[0:1] offset:32
	global_load_dwordx4 v[156:159], v154, s[0:1] offset:64
	global_load_dwordx4 v[160:163], v154, s[0:1] offset:96
	global_load_dwordx4 v[164:167], v154, s[0:1] offset:128
	global_load_dwordx4 v[168:171], v154, s[0:1] offset:160
	s_movk_i32 s4, 0x410
	v_lshlrev_b32_e32 v130, 1, v130
	v_mul_lo_u32 v131, v206, s4
	v_add3_u32 v155, 0, v130, v131
	global_load_dwordx4 v[172:175], v154, s[0:1] offset:192
	global_load_dwordx4 v[146:149], v154, s[0:1] offset:224
	global_load_dwordx4 v[142:145], v154, s[0:1] offset:256
	global_load_dwordx4 v[130:133], v154, s[0:1] offset:288
	global_load_dwordx4 v[138:141], v154, s[0:1] offset:320
	v_add_u32_e32 v176, 0x8000, v155
	s_waitcnt vmcnt(10)
	v_pk_add_f32 v[114:115], v[134:135], v[114:115]
	v_pk_add_f32 v[116:117], v[136:137], v[116:117]
	v_pk_add_f32 v[98:99], v[134:135], v[98:99]
	v_pk_add_f32 v[100:101], v[136:137], v[100:101]
	s_waitcnt vmcnt(9)
	v_pk_add_f32 v[118:119], v[150:151], v[118:119]
	v_pk_add_f32 v[120:121], v[152:153], v[120:121]
	s_waitcnt vmcnt(6)
	v_pk_add_f32 v[82:83], v[164:165], v[82:83]
	v_pk_add_f32 v[84:85], v[166:167], v[84:85]
	v_pk_add_f32 v[66:67], v[164:165], v[66:67]
	v_pk_add_f32 v[68:69], v[166:167], v[68:69]
	s_waitcnt vmcnt(5)
	v_pk_add_f32 v[70:71], v[168:169], v[70:71]
	v_pk_add_f32 v[72:73], v[170:171], v[72:73]
	v_pk_add_f32 v[102:103], v[150:151], v[102:103]
	v_pk_add_f32 v[104:105], v[152:153], v[104:105]
	v_pk_add_f32 v[122:123], v[156:157], v[122:123]
	v_pk_add_f32 v[124:125], v[158:159], v[124:125]
	v_pk_add_f32 v[106:107], v[156:157], v[106:107]
	v_pk_add_f32 v[108:109], v[158:159], v[108:109]
	v_pk_add_f32 v[126:127], v[160:161], v[126:127]
	v_pk_add_f32 v[128:129], v[162:163], v[128:129]
	v_pk_add_f32 v[110:111], v[160:161], v[110:111]
	v_pk_add_f32 v[112:113], v[162:163], v[112:113]
	v_pk_add_f32 v[86:87], v[168:169], v[86:87]
	v_pk_add_f32 v[88:89], v[170:171], v[88:89]
	v_cvt_pk_f16_f32 v114, v114, v115
	v_cvt_pk_f16_f32 v115, v116, v117
	v_cvt_pk_f16_f32 v98, v98, v99
	v_cvt_pk_f16_f32 v99, v100, v101
	v_cvt_pk_f16_f32 v100, v118, v119
	v_cvt_pk_f16_f32 v101, v120, v121
	v_cvt_pk_f16_f32 v82, v82, v83
	v_cvt_pk_f16_f32 v83, v84, v85
	v_cvt_pk_f16_f32 v84, v66, v67
	v_cvt_pk_f16_f32 v85, v68, v69
	v_cvt_pk_f16_f32 v70, v70, v71
	v_cvt_pk_f16_f32 v71, v72, v73
	v_cvt_pk_f16_f32 v102, v102, v103
	v_cvt_pk_f16_f32 v103, v104, v105
	v_cvt_pk_f16_f32 v104, v122, v123
	v_cvt_pk_f16_f32 v105, v124, v125
	v_cvt_pk_f16_f32 v106, v106, v107
	v_cvt_pk_f16_f32 v107, v108, v109
	v_cvt_pk_f16_f32 v108, v126, v127
	v_cvt_pk_f16_f32 v109, v128, v129
	v_cvt_pk_f16_f32 v110, v110, v111
	v_cvt_pk_f16_f32 v111, v112, v113
	v_cvt_pk_f16_f32 v86, v86, v87
	ds_write2_b64 v155, v[114:115], v[100:101] offset1:2
	ds_write2_b64 v176, v[98:99], v[102:103] offset0:64 offset1:66
	ds_write2_b64 v155, v[104:105], v[108:109] offset0:4 offset1:6
	ds_write2_b64 v176, v[106:107], v[110:111] offset0:68 offset1:70
	v_cvt_pk_f16_f32 v87, v88, v89
	ds_write2_b64 v176, v[84:85], v[70:71] offset0:72 offset1:74
	s_waitcnt vmcnt(4)
	v_pk_add_f32 v[70:71], v[172:173], v[90:91]
	v_pk_add_f32 v[84:85], v[174:175], v[92:93]
	v_pk_add_f32 v[74:75], v[172:173], v[74:75]
	ds_write2_b64 v155, v[82:83], v[86:87] offset0:8 offset1:10
	v_mov_b64_e32 v[82:83], v[70:71]
	global_load_dwordx4 v[66:69], v154, s[0:1] offset:352
	global_load_dwordx4 v[70:73], v154, s[0:1] offset:384
	v_cvt_pk_f16_f32 v82, v82, v83
	v_cvt_pk_f16_f32 v83, v84, v85
	v_cvt_pk_f16_f32 v84, v74, v75
	v_pk_add_f32 v[74:75], v[174:175], v[76:77]
	s_waitcnt vmcnt(5)
	v_pk_add_f32 v[78:79], v[146:147], v[78:79]
	v_cvt_pk_f16_f32 v85, v74, v75
	global_load_dwordx4 v[74:77], v154, s[0:1] offset:416
	v_pk_add_f32 v[80:81], v[148:149], v[80:81]
	v_cvt_pk_f16_f32 v78, v78, v79
	v_cvt_pk_f16_f32 v79, v80, v81
	ds_write2_b64 v176, v[84:85], v[78:79] offset0:76 offset1:78
	global_load_dwordx4 v[78:81], v154, s[0:1] offset:448
	v_pk_add_f32 v[86:87], v[146:147], v[94:95]
	v_pk_add_f32 v[88:89], v[148:149], v[96:97]
	s_waitcnt vmcnt(6)
	v_pk_add_f32 v[50:51], v[142:143], v[50:51]
	v_pk_add_f32 v[52:53], v[144:145], v[52:53]
	v_pk_add_f32 v[34:35], v[142:143], v[34:35]
	v_cvt_pk_f16_f32 v86, v86, v87
	v_cvt_pk_f16_f32 v87, v88, v89
	v_cvt_pk_f16_f32 v50, v50, v51
	v_cvt_pk_f16_f32 v51, v52, v53
	v_cvt_pk_f16_f32 v52, v34, v35
	v_pk_add_f32 v[34:35], v[144:145], v[36:37]
	ds_write2_b64 v155, v[82:83], v[86:87] offset0:12 offset1:14
	v_mov_b64_e32 v[82:83], v[34:35]
	global_load_dwordx4 v[34:37], v154, s[0:1] offset:480
	s_waitcnt vmcnt(6)
	v_pk_add_f32 v[38:39], v[130:131], v[38:39]
	v_pk_add_f32 v[40:41], v[132:133], v[40:41]
	v_cvt_pk_f16_f32 v53, v82, v83
	v_cvt_pk_f16_f32 v38, v38, v39
	v_cvt_pk_f16_f32 v39, v40, v41
	ds_write2_b64 v176, v[52:53], v[38:39] offset0:80 offset1:82
	s_waitcnt vmcnt(5)
	v_pk_add_f32 v[38:39], v[138:139], v[58:59]
	v_pk_add_f32 v[40:41], v[140:141], v[60:61]
	v_cvt_pk_f16_f32 v38, v38, v39
	v_cvt_pk_f16_f32 v39, v40, v41
	v_pk_add_f32 v[40:41], v[138:139], v[42:43]
	v_pk_add_f32 v[42:43], v[140:141], v[44:45]
	v_cvt_pk_f16_f32 v40, v40, v41
	v_cvt_pk_f16_f32 v41, v42, v43
	v_pk_add_f32 v[54:55], v[130:131], v[54:55]
	v_pk_add_f32 v[56:57], v[132:133], v[56:57]
	v_cmp_gt_u32_e64 s[0:1], 8, v0
	v_cvt_pk_f16_f32 v54, v54, v55
	v_cvt_pk_f16_f32 v55, v56, v57
	s_and_b64 s[6:7], s[20:21], s[0:1]
	ds_write2_b64 v155, v[50:51], v[54:55] offset0:16 offset1:18
	s_waitcnt vmcnt(4)
	v_pk_add_f32 v[42:43], v[66:67], v[62:63]
	s_waitcnt vmcnt(3)
	v_pk_add_f32 v[18:19], v[70:71], v[18:19]
	v_pk_add_f32 v[20:21], v[72:73], v[20:21]
	v_pk_add_f32 v[2:3], v[70:71], v[2:3]
	v_pk_add_f32 v[4:5], v[72:73], v[4:5]
	v_cvt_pk_f16_f32 v18, v18, v19
	v_cvt_pk_f16_f32 v19, v20, v21
	v_cvt_pk_f16_f32 v2, v2, v3
	v_cvt_pk_f16_f32 v3, v4, v5
	s_waitcnt vmcnt(2)
	v_pk_add_f32 v[4:5], v[74:75], v[22:23]
	v_pk_add_f32 v[20:21], v[76:77], v[24:25]
	v_cvt_pk_f16_f32 v4, v4, v5
	v_cvt_pk_f16_f32 v5, v20, v21
	ds_write2_b64 v155, v[18:19], v[4:5] offset0:24 offset1:26
	v_pk_add_f32 v[4:5], v[74:75], v[6:7]
	v_pk_add_f32 v[6:7], v[76:77], v[8:9]
	v_cvt_pk_f16_f32 v4, v4, v5
	v_cvt_pk_f16_f32 v5, v6, v7
	ds_write2_b64 v176, v[2:3], v[4:5] offset0:88 offset1:90
	s_waitcnt vmcnt(1)
	v_pk_add_f32 v[2:3], v[78:79], v[26:27]
	v_pk_add_f32 v[4:5], v[80:81], v[28:29]
	v_cvt_pk_f16_f32 v2, v2, v3
	v_cvt_pk_f16_f32 v3, v4, v5
	v_pk_add_f32 v[4:5], v[78:79], v[10:11]
	v_pk_add_f32 v[6:7], v[80:81], v[12:13]
	v_pk_add_f32 v[44:45], v[68:69], v[64:65]
	v_cvt_pk_f16_f32 v4, v4, v5
	v_cvt_pk_f16_f32 v5, v6, v7
	s_waitcnt vmcnt(0)
	v_pk_add_f32 v[6:7], v[34:35], v[30:31]
	v_pk_add_f32 v[8:9], v[36:37], v[32:33]
	v_cvt_pk_f16_f32 v42, v42, v43
	v_cvt_pk_f16_f32 v43, v44, v45
	v_cvt_pk_f16_f32 v6, v6, v7
	v_cvt_pk_f16_f32 v7, v8, v9
	ds_write2_b64 v155, v[38:39], v[42:43] offset0:20 offset1:22
	v_pk_add_f32 v[38:39], v[66:67], v[46:47]
	v_pk_add_f32 v[42:43], v[68:69], v[48:49]
	ds_write2_b64 v155, v[2:3], v[6:7] offset0:28 offset1:30
	v_pk_add_f32 v[2:3], v[34:35], v[14:15]
	v_pk_add_f32 v[6:7], v[36:37], v[16:17]
	v_cvt_pk_f16_f32 v38, v38, v39
	v_cvt_pk_f16_f32 v39, v42, v43
	v_cvt_pk_f16_f32 v2, v2, v3
	v_cvt_pk_f16_f32 v3, v6, v7
	ds_write2_b64 v176, v[40:41], v[38:39] offset0:84 offset1:86
	ds_write2_b64 v176, v[4:5], v[2:3] offset0:92 offset1:94
	s_branch .Lepi_join
